# static s_setprio 1 for the younger wave half (waves 4-7) across the mixer phases, reset before the out-projection GEMM
# speedup vs baseline: 1.0045x; 1.0045x over previous
; template <int GRP>
; __device__ __forceinline__ void conv_item(Frame& F, int r) {
;     unsigned char* scr = F.glds + F.wave * 8704; unsigned char* ws = F.ws;
;     float* cmx = (float*)(ws + WS_CTL + COLMAX_OFF);
;     if (GRP == 0 || GRP == 1 || GRP == 2 || GRP == 4) {
;         constexpr int l = (GRP == 2 || GRP == 4) ? 1 : 0;
;         constexpr bool QUANT = (GRP == 1 || GRP == 4); constexpr int NI = QUANT ? CI_WI : CS_WI;
;         if (r < NI) { const int kb = r / 152, nb = r % 152, c0 = (nb < 112) ? nb * 32 : SRC_GATE + 8 + (nb - 112) * 32, drow = nb * 32;
;             if (QUANT) cvt_item_i8(inptr(F, IN_WIN) + (size_t)l * D * NIN_SRC, NIN_SRC, kb * 128, c0, ws + WS_WIN + (size_t)l * NIN * D, D, drow, cmx + CMX_WIN + l * NIN + drow, scr, F.lane);
;             else colmax_item(inptr(F, IN_WIN) + (size_t)l * D * NIN_SRC, NIN_SRC, kb * 128, c0, cmx + CMX_WIN + l * NIN + drow, F.lane);
;             return; }
;         r -= NI;
;     }
;     if (GRP == 0 || GRP == 2) {
;         constexpr int l = (GRP == 2) ? 1 : 0;
;         if (r < CI_WO) { const int kb = r / 64, nb = r % 64;
;             cvt_item8(inptr(F, IN_WOUT) + (size_t)l * D * D, D, kb * 128, nb * 32, ws + WS_WOUT + (size_t)l * D * D, D, nb * 32, scr, F.lane); return; }
;         r -= CI_WO;
;         if (GRP == 0) {
;             if (r < CI_FD) { const int kb = r / 64, nb = r % 64; cvt_item8(inptr(F, IN_FD), D, kb * 128, nb * 32, ws + WS_WD, DFF, nb * 32, scr, F.lane); return; }
;             r -= CI_FD;
;         } else {
;             if (r < CI_MD) { const int e = r / (22 * 64); r %= (22 * 64); const int kb = r / 64, nb = r % 64;
;                 cvt_item8(inptr(F, IN_MD) + (size_t)e * DFE * D, D, kb * 128, nb * 32, ws + WS_MD + (size_t)e * D * DFE, DFE, nb * 32, scr, F.lane); return; }
;             r -= CI_MD;
;         }
;     }
; template <int L>
; __device__ __forceinline__ void layer(Frame& F, const XcdBarrier& bar, float* out, const int lo, const int hi) {
;     ...
;         if (cls == 0) { conv_all<GRP>(F, (F.G == 256) ? ((L == 0) ? SLOT_FIRST0 : SLOT_FIRST1) : 0); if (L == 0 && F.G == 256) { const int e4 = F.gw - G4_SLACK0; if (e4 >= 0 && e4 < G4_TAIL) conv_item<4>(F, 2048 + e4); } __syncthreads(); }
.LBB0_503:
	s_or_b64 exec, exec, s[0:1]
	v_readlane_b32 s0, v255, 9
	s_cmp_lt_u32 s0, 4
	s_cbranch_scc1 .Lprio_4
	s_setprio 1
.Lprio_4:
	v_readlane_b32 s0, v255, 27
	s_cmp_lg_u32 s0, 0
	s_waitcnt lgkmcnt(0)
	s_barrier
	s_cbranch_scc1 .LBB0_527
	s_cmpk_eq_i32 s48, 0x100
	s_cselect_b64 s[0:1], -1, 0
	s_and_b64 s[6:7], s[0:1], exec
	s_cselect_b32 s3, 0x15b0, 0
	v_readlane_b32 s4, v255, 10
	s_add_i32 s3, s3, s4
	s_cmpk_gt_i32 s3, 0x3c2f
	s_cbranch_scc1 .LBB0_524
	v_readlane_b32 s4, v255, 9
	s_mulk_i32 s4, 0x2200
	v_lshrrev_b32_e32 v1, 1, v0
	v_mov_b32_e32 v11, 0
	v_lshlrev_b32_e32 v10, 4, v194
	s_add_i32 s4, s4, 0
	v_and_b32_e32 v15, 28, v1
	v_lshl_add_u64 v[6:7], s[50:51], 0, v[10:11]
	s_mov_b64 s[10:11], 0xbbc00
	v_and_b32_e32 v1, 7, v0
	v_lshl_add_u64 v[12:13], v[6:7], 0, s[10:11]
	s_add_u32 s10, s50, 0x8b000
	v_lshlrev_b32_e32 v14, 2, v1
	v_mul_u32_u24_e32 v23, 0x210, v1
	v_lshlrev_b32_e32 v16, 4, v1
	v_mbcnt_lo_u32_b32 v1, -1, 0
	v_lshlrev_b32_e32 v2, 2, v194
	s_addc_u32 s11, s51, 0
	v_lshrrev_b32_e32 v20, 3, v194
	v_mov_b32_e32 v17, v11
	v_mbcnt_hi_u32_b32 v30, -1, v1
	v_and_b32_e32 v4, 28, v2
	s_add_u32 s12, s50, 0x13200000
	v_lshlrev_b32_e32 v21, 2, v20
	v_lshl_add_u64 v[6:7], s[50:51], 0, v[16:17]
	s_mov_b64 s[14:15], 0x3400000
	v_readlane_b32 s8, v255, 13
	v_and_b32_e32 v1, 64, v30
	s_mov_b32 s9, 0
	v_cmp_gt_u32_e64 s[6:7], 8, v194
	s_addc_u32 s13, s51, 0
	v_add_u32_e32 v22, s4, v21
	v_add_u32_e32 v24, s4, v16
	v_mul_u32_u24_e32 v25, 0x84, v20
	v_or_b32_e32 v26, 8, v20
	v_or_b32_e32 v27, 16, v20
	v_or_b32_e32 v28, 24, v20
	v_lshl_add_u64 v[18:19], v[6:7], 0, s[14:15]
	s_lshl_b32 s4, s3, 5
	s_lshl_b32 s22, s8, 5
	s_add_i32 s23, 0, 0x20240
	s_movk_i32 s24, 0x4c20
	s_movk_i32 s25, 0xa0
	s_movk_i32 s26, 0x2000
	s_movk_i32 s27, 0x5000
	s_mov_b32 s28, 0x8000
	s_mov_b32 s29, 0x58000
	s_mov_b32 s30, 0x5a000
	s_mov_b32 s31, 0x5d000
	s_mov_b32 s34, 0x60000
	s_mov_b32 s35, 0xb0000
	s_mov_b32 s36, 0xb2000
	s_mov_b32 s37, 0xb5000
	s_mov_b32 s38, 0xb8000
	s_mov_b32 s39, 0x108000
	s_mov_b32 s40, 0x10a000
	s_mov_b32 s41, 0x10d000
	s_mov_b32 s42, 0x110000
	v_lshlrev_b32_e32 v29, 2, v2
	s_add_i32 s43, 0, 0x202b0
	s_movk_i32 s44, 0x4000
	s_movk_i32 s45, 0x6000
	s_mov_b32 s46, 0x40000
	s_mov_b32 s47, 0x42000
	s_mov_b32 s49, 0x44000
	s_mov_b32 s52, 0x46000
	s_mov_b32 s53, 0x80000
	s_mov_b32 s54, 0x82000
	s_mov_b32 s55, 0x84000
	s_mov_b32 s56, 0x86000
	s_mov_b32 s57, 0xc0000
	s_mov_b32 s62, 0xc2000
	s_mov_b32 s63, 0xc4000
	s_mov_b32 s66, 0xc6000
	s_mov_b32 s67, 0xc3e00000
	s_add_i32 s68, 0, 0x20248
	s_mov_b64 s[14:15], 0x1000000
	v_lshlrev_b32_e32 v10, 2, v4
	v_xor_b32_e32 v31, 8, v30
	v_add_u32_e32 v32, 64, v1
	v_xor_b32_e32 v33, 16, v30
	s_waitcnt vmcnt(14)
	v_xor_b32_e32 v34, 32, v30
	v_mov_b32_e32 v35, 0x580000
	v_mov_b32_e32 v36, 0x1600
	v_mov_b32_e32 v37, 0x43e00000
	v_readlane_b32 s16, v255, 9
	s_cmp_lt_u32 s16, 4
	s_cbranch_scc1 .Lstg_507
	s_sleep 44

; #define SEAM(k) do { if (IN(k) && IN((k) + 1)) GRID_BAR(); } while (0)
; template <int L>
; __device__ __forceinline__ void layer(Frame& F, const XcdBarrier& bar, float* out, const int lo, const int hi) {
;     ...
;         __syncthreads();
;         if (cls == 3) { conv_all<GRP>(F, (F.G == 256) ? ((L == 0) ? SLOT_FIRST0 : SLOT_FIRST1) : 0); if (L == 0 && F.G == 256) { const int e4 = F.gw - G4_SLACK0; if (e4 >= 0 && e4 < G4_TAIL) conv_item<4>(F, 2048 + e4); } __syncthreads(); }
;     }
;     SEAM(pb + 2);
.LBB0_999:
	s_or_b64 exec, exec, s[0:1]
	s_setprio 0
	s_waitcnt lgkmcnt(0)
	s_barrier

; template <int GRP>
; __device__ __forceinline__ void conv_item(Frame& F, int r) {
;     unsigned char* scr = F.glds + F.wave * 8704; unsigned char* ws = F.ws;
;     float* cmx = (float*)(ws + WS_CTL + COLMAX_OFF);
;     if (GRP == 0 || GRP == 1 || GRP == 2 || GRP == 4) {
;         constexpr int l = (GRP == 2 || GRP == 4) ? 1 : 0;
;         constexpr bool QUANT = (GRP == 1 || GRP == 4); constexpr int NI = QUANT ? CI_WI : CS_WI;
;         if (r < NI) { const int kb = r / 152, nb = r % 152, c0 = (nb < 112) ? nb * 32 : SRC_GATE + 8 + (nb - 112) * 32, drow = nb * 32;
;             if (QUANT) cvt_item_i8(inptr(F, IN_WIN) + (size_t)l * D * NIN_SRC, NIN_SRC, kb * 128, c0, ws + WS_WIN + (size_t)l * NIN * D, D, drow, cmx + CMX_WIN + l * NIN + drow, scr, F.lane);
;             else colmax_item(inptr(F, IN_WIN) + (size_t)l * D * NIN_SRC, NIN_SRC, kb * 128, c0, cmx + CMX_WIN + l * NIN + drow, F.lane);
;             return; }
;         r -= NI;
;     }
;     if (GRP == 0 || GRP == 2) {
;         constexpr int l = (GRP == 2) ? 1 : 0;
;         if (r < CI_WO) { const int kb = r / 64, nb = r % 64;
;             cvt_item8(inptr(F, IN_WOUT) + (size_t)l * D * D, D, kb * 128, nb * 32, ws + WS_WOUT + (size_t)l * D * D, D, nb * 32, scr, F.lane); return; }
;         r -= CI_WO;
;         if (GRP == 0) {
;             if (r < CI_FD) { const int kb = r / 64, nb = r % 64; cvt_item8(inptr(F, IN_FD), D, kb * 128, nb * 32, ws + WS_WD, DFF, nb * 32, scr, F.lane); return; }
;             r -= CI_FD;
;         } else {
;             if (r < CI_MD) { const int e = r / (22 * 64); r %= (22 * 64); const int kb = r / 64, nb = r % 64;
;                 cvt_item8(inptr(F, IN_MD) + (size_t)e * DFE * D, D, kb * 128, nb * 32, ws + WS_MD + (size_t)e * D * DFE, DFE, nb * 32, scr, F.lane); return; }
;             r -= CI_MD;
;         }
;     }
; template <int L>
; __device__ __forceinline__ void layer(Frame& F, const XcdBarrier& bar, float* out, const int lo, const int hi) {
;     ...
;         if (cls == 0) { conv_all<GRP>(F, (F.G == 256) ? ((L == 0) ? SLOT_FIRST0 : SLOT_FIRST1) : 0); if (L == 0 && F.G == 256) { const int e4 = F.gw - G4_SLACK0; if (e4 >= 0 && e4 < G4_TAIL) conv_item<4>(F, 2048 + e4); } __syncthreads(); }
.Lprio_13:
	v_readlane_b32 s0, v255, 27
	s_cmp_lg_u32 s0, 0
	s_waitcnt lgkmcnt(0)
	s_barrier
	s_cbranch_scc1 .LBB0_1674
	s_cmpk_eq_i32 s48, 0x100
	s_cselect_b32 s0, 0x1800, 0
	v_readlane_b32 s1, v255, 10
	s_add_i32 s3, s0, s1
	s_cmpk_gt_i32 s3, 0x57ff
	v_readlane_b32 s40, v255, 13
	s_cbranch_scc1 .LBB0_1673
	v_readlane_b32 s0, v255, 9
	s_mulk_i32 s0, 0x2200
	s_add_i32 s0, s0, 0
	v_and_b32_e32 v2, 7, v0
	s_add_u32 s4, s50, 0x8200000
	v_lshrrev_b32_e32 v1, 3, v194
	v_lshlrev_b32_e32 v4, 2, v2
	v_mul_u32_u24_e32 v7, 0x210, v2
	v_lshlrev_b32_e32 v2, 4, v2
	s_addc_u32 s12, s51, 0
	v_lshlrev_b32_e32 v16, 2, v1
	v_add_u32_e32 v8, s0, v2
	v_mul_u32_u24_e32 v9, 0x84, v1
	s_add_u32 s13, s50, 0x8b000
	v_mov_b32_e32 v3, 0
	v_add_u32_e32 v6, s0, v16
	v_add_u32_e32 v22, v8, v9
	s_addc_u32 s14, s51, 0
	v_or_b32_e32 v17, 8, v1
	v_or_b32_e32 v18, 16, v1
	v_or_b32_e32 v19, 24, v1
	s_movk_i32 s15, 0xa0
	v_lshlrev_b32_e32 v4, 2, v4
	v_mov_b32_e32 v5, v3
	s_mov_b32 s16, 0x42fe0000
	s_movk_i32 s17, 0x2000
	s_movk_i32 s18, 0x5000
	s_mov_b32 s19, 0x8000
	s_mov_b32 s20, 0x58000
	s_mov_b32 s21, 0x5a000
	s_mov_b32 s22, 0x5d000
	s_mov_b32 s23, 0x60000
	s_mov_b32 s24, 0xb0000
	s_mov_b32 s25, 0xb2000
	s_mov_b32 s26, 0xb5000
	s_mov_b32 s27, 0xb8000
	s_mov_b32 s28, 0x108000
	s_mov_b32 s29, 0x10a000
	s_mov_b32 s30, 0x10d000
	s_mov_b32 s31, 0x110000
	s_mov_b32 s34, 0xc2fe0000
	v_mov_b32_e32 v20, 0x42fe0000
	s_mov_b32 s35, 0xc0c0500
	v_add_u32_e32 v21, v6, v7
	v_add_u32_e32 v23, 0x420, v22
	v_add_u32_e32 v24, 0x428, v22
	v_add_u32_e32 v25, 0x840, v22
	v_add_u32_e32 v26, 0x848, v22
	v_add_u32_e32 v27, 0xc60, v22
	v_add_u32_e32 v28, 0xc68, v22
	v_readlane_b32 s0, v255, 9
	s_cmp_lt_u32 s0, 4
	s_cbranch_scc1 .Lstg_1672
	s_sleep 44
